# k_l2: 16-byte record loads (2 records per lane) and 16-byte stores in the copy-out; plus row-length ranking in the spmm kernels
# speedup vs baseline: 1.0570x; 1.0067x over previous
.LBB3_46:
	s_and_b64 vcc, exec, s[0:1]
	s_cbranch_vccz .LBB3_141
	s_ashr_i32 s37, s36, 31
	s_lshl_b64 s[0:1], s[36:37], 3
	s_add_u32 s0, s2, s0
	s_addc_u32 s1, s3, s1
	s_mov_b32 s6, 0x20000
	s_add_i32 s8, s44, 31
	s_lshr_b32 s8, s8, 5
	s_add_i32 s8, s8, -1
	s_lshl_b32 s9, s42, 2
	s_sub_i32 s8, s8, s9
	s_bfe_u32 s8, s8, 0x1000a
	s_mul_i32 s8, s8, 31
	v_mov_b32_e32 v66, 0
	v_mov_b32_e32 v67, 0
	v_mov_b32_e32 v68, 0
	v_mov_b32_e32 v69, 0
	v_lshl_add_u32 v1, v0, 4, s6
	ds_write_b128 v1, v[66:69]
	v_mov_b32_e32 v79, 1
	v_add_u32_e32 v76, 0, v0
	v_lshlrev_b32_e32 v76, 1, v76
	v_cmp_gt_i32_e32 vcc, s33, v76
	v_lshlrev_b32_e32 v76, 3, v76
	s_and_saveexec_b64 s[4:5], vcc
	global_load_dwordx4 v[2:5], v76, s[0:1] nt
	s_or_b64 exec, exec, s[4:5]
	v_add_u32_e32 v76, 1024, v0
	v_lshlrev_b32_e32 v76, 1, v76
	v_cmp_gt_i32_e32 vcc, s33, v76
	v_lshlrev_b32_e32 v76, 3, v76
	s_and_saveexec_b64 s[4:5], vcc
	global_load_dwordx4 v[6:9], v76, s[0:1] nt
	s_or_b64 exec, exec, s[4:5]
	v_add_u32_e32 v76, 2048, v0
	v_lshlrev_b32_e32 v76, 1, v76
	v_cmp_gt_i32_e32 vcc, s33, v76
	v_lshlrev_b32_e32 v76, 3, v76
	s_and_saveexec_b64 s[4:5], vcc
	global_load_dwordx4 v[10:13], v76, s[0:1] nt
	s_or_b64 exec, exec, s[4:5]
	v_add_u32_e32 v76, 3072, v0
	v_lshlrev_b32_e32 v76, 1, v76
	v_cmp_gt_i32_e32 vcc, s33, v76
	v_lshlrev_b32_e32 v76, 3, v76
	s_and_saveexec_b64 s[4:5], vcc
	global_load_dwordx4 v[14:17], v76, s[0:1] nt
	s_or_b64 exec, exec, s[4:5]
	v_add_u32_e32 v76, 4096, v0
	v_lshlrev_b32_e32 v76, 1, v76
	v_cmp_gt_i32_e32 vcc, s33, v76
	v_lshlrev_b32_e32 v76, 3, v76
	s_and_saveexec_b64 s[4:5], vcc
	global_load_dwordx4 v[18:21], v76, s[0:1] nt
	s_or_b64 exec, exec, s[4:5]
	v_add_u32_e32 v76, 5120, v0
	v_lshlrev_b32_e32 v76, 1, v76
	v_cmp_gt_i32_e32 vcc, s33, v76
	v_lshlrev_b32_e32 v76, 3, v76
	s_and_saveexec_b64 s[4:5], vcc
	global_load_dwordx4 v[22:25], v76, s[0:1] nt
	s_or_b64 exec, exec, s[4:5]
	v_add_u32_e32 v76, 6144, v0
	v_lshlrev_b32_e32 v76, 1, v76
	v_cmp_gt_i32_e32 vcc, s33, v76
	v_lshlrev_b32_e32 v76, 3, v76
	s_and_saveexec_b64 s[4:5], vcc
	global_load_dwordx4 v[26:29], v76, s[0:1] nt
	s_or_b64 exec, exec, s[4:5]
	v_add_u32_e32 v76, 7168, v0
	v_lshlrev_b32_e32 v76, 1, v76
	v_cmp_gt_i32_e32 vcc, s33, v76
	v_lshlrev_b32_e32 v76, 3, v76
	s_and_saveexec_b64 s[4:5], vcc
	global_load_dwordx4 v[30:33], v76, s[0:1] nt
	s_or_b64 exec, exec, s[4:5]
	s_waitcnt lgkmcnt(0)
	s_barrier
	s_waitcnt vmcnt(7)
	v_add_u32_e32 v76, 0, v0
	v_lshl_add_u32 v76, v76, 1, 0
	v_cmp_gt_i32_e32 vcc, s33, v76
	v_lshrrev_b32_e32 v76, 25, v2
	v_bfe_u32 v77, v2, 13, 12
	v_min_u32_e32 v77, 31, v77
	v_xor_b32_e32 v77, s8, v77
	v_lshl_or_b32 v76, v76, 5, v77
	v_lshl_add_u32 v50, v76, 2, s6
	s_and_saveexec_b64 s[4:5], vcc
	ds_add_rtn_u32 v34, v50, v79
	s_or_b64 exec, exec, s[4:5]
	s_waitcnt vmcnt(7)
	v_add_u32_e32 v76, 0, v0
	v_lshl_add_u32 v76, v76, 1, 1
	v_cmp_gt_i32_e32 vcc, s33, v76
	v_lshrrev_b32_e32 v76, 25, v4
	v_bfe_u32 v77, v4, 13, 12
	v_min_u32_e32 v77, 31, v77
	v_xor_b32_e32 v77, s8, v77
	v_lshl_or_b32 v76, v76, 5, v77
	v_lshl_add_u32 v51, v76, 2, s6
	s_and_saveexec_b64 s[4:5], vcc
	ds_add_rtn_u32 v35, v51, v79
	s_or_b64 exec, exec, s[4:5]
	s_waitcnt vmcnt(6)
	v_add_u32_e32 v76, 1024, v0
	v_lshl_add_u32 v76, v76, 1, 0
	v_cmp_gt_i32_e32 vcc, s33, v76
	v_lshrrev_b32_e32 v76, 25, v6
	v_bfe_u32 v77, v6, 13, 12
	v_min_u32_e32 v77, 31, v77
	v_xor_b32_e32 v77, s8, v77
	v_lshl_or_b32 v76, v76, 5, v77
	v_lshl_add_u32 v52, v76, 2, s6
	s_and_saveexec_b64 s[4:5], vcc
	ds_add_rtn_u32 v36, v52, v79
	s_or_b64 exec, exec, s[4:5]
	s_waitcnt vmcnt(6)
	v_add_u32_e32 v76, 1024, v0
	v_lshl_add_u32 v76, v76, 1, 1
	v_cmp_gt_i32_e32 vcc, s33, v76
	v_lshrrev_b32_e32 v76, 25, v8
	v_bfe_u32 v77, v8, 13, 12
	v_min_u32_e32 v77, 31, v77
	v_xor_b32_e32 v77, s8, v77
	v_lshl_or_b32 v76, v76, 5, v77
	v_lshl_add_u32 v53, v76, 2, s6
	s_and_saveexec_b64 s[4:5], vcc
	ds_add_rtn_u32 v37, v53, v79
	s_or_b64 exec, exec, s[4:5]
	s_waitcnt vmcnt(5)
	v_add_u32_e32 v76, 2048, v0
	v_lshl_add_u32 v76, v76, 1, 0
	v_cmp_gt_i32_e32 vcc, s33, v76
	v_lshrrev_b32_e32 v76, 25, v10
	v_bfe_u32 v77, v10, 13, 12
	v_min_u32_e32 v77, 31, v77
	v_xor_b32_e32 v77, s8, v77
	v_lshl_or_b32 v76, v76, 5, v77
	v_lshl_add_u32 v54, v76, 2, s6
	s_and_saveexec_b64 s[4:5], vcc
	ds_add_rtn_u32 v38, v54, v79
	s_or_b64 exec, exec, s[4:5]
	s_waitcnt vmcnt(5)
	v_add_u32_e32 v76, 2048, v0
	v_lshl_add_u32 v76, v76, 1, 1
	v_cmp_gt_i32_e32 vcc, s33, v76
	v_lshrrev_b32_e32 v76, 25, v12
	v_bfe_u32 v77, v12, 13, 12
	v_min_u32_e32 v77, 31, v77
	v_xor_b32_e32 v77, s8, v77
	v_lshl_or_b32 v76, v76, 5, v77
	v_lshl_add_u32 v55, v76, 2, s6
	s_and_saveexec_b64 s[4:5], vcc
	ds_add_rtn_u32 v39, v55, v79
	s_or_b64 exec, exec, s[4:5]
	s_waitcnt vmcnt(4)
	v_add_u32_e32 v76, 3072, v0
	v_lshl_add_u32 v76, v76, 1, 0
	v_cmp_gt_i32_e32 vcc, s33, v76
	v_lshrrev_b32_e32 v76, 25, v14
	v_bfe_u32 v77, v14, 13, 12
	v_min_u32_e32 v77, 31, v77
	v_xor_b32_e32 v77, s8, v77
	v_lshl_or_b32 v76, v76, 5, v77
	v_lshl_add_u32 v56, v76, 2, s6
	s_and_saveexec_b64 s[4:5], vcc
	ds_add_rtn_u32 v40, v56, v79
	s_or_b64 exec, exec, s[4:5]
	s_waitcnt vmcnt(4)
	v_add_u32_e32 v76, 3072, v0
	v_lshl_add_u32 v76, v76, 1, 1
	v_cmp_gt_i32_e32 vcc, s33, v76
	v_lshrrev_b32_e32 v76, 25, v16
	v_bfe_u32 v77, v16, 13, 12
	v_min_u32_e32 v77, 31, v77
	v_xor_b32_e32 v77, s8, v77
	v_lshl_or_b32 v76, v76, 5, v77
	v_lshl_add_u32 v57, v76, 2, s6
	s_and_saveexec_b64 s[4:5], vcc
	ds_add_rtn_u32 v41, v57, v79
	s_or_b64 exec, exec, s[4:5]
	s_waitcnt vmcnt(3)
	v_add_u32_e32 v76, 4096, v0
	v_lshl_add_u32 v76, v76, 1, 0
	v_cmp_gt_i32_e32 vcc, s33, v76
	v_lshrrev_b32_e32 v76, 25, v18
	v_bfe_u32 v77, v18, 13, 12
	v_min_u32_e32 v77, 31, v77
	v_xor_b32_e32 v77, s8, v77
	v_lshl_or_b32 v76, v76, 5, v77
	v_lshl_add_u32 v58, v76, 2, s6
	s_and_saveexec_b64 s[4:5], vcc
	ds_add_rtn_u32 v42, v58, v79
	s_or_b64 exec, exec, s[4:5]
	s_waitcnt vmcnt(3)
	v_add_u32_e32 v76, 4096, v0
	v_lshl_add_u32 v76, v76, 1, 1
	v_cmp_gt_i32_e32 vcc, s33, v76
	v_lshrrev_b32_e32 v76, 25, v20
	v_bfe_u32 v77, v20, 13, 12
	v_min_u32_e32 v77, 31, v77
	v_xor_b32_e32 v77, s8, v77
	v_lshl_or_b32 v76, v76, 5, v77
	v_lshl_add_u32 v59, v76, 2, s6
	s_and_saveexec_b64 s[4:5], vcc
	ds_add_rtn_u32 v43, v59, v79
	s_or_b64 exec, exec, s[4:5]
	s_waitcnt vmcnt(2)
	v_add_u32_e32 v76, 5120, v0
	v_lshl_add_u32 v76, v76, 1, 0
	v_cmp_gt_i32_e32 vcc, s33, v76
	v_lshrrev_b32_e32 v76, 25, v22
	v_bfe_u32 v77, v22, 13, 12
	v_min_u32_e32 v77, 31, v77
	v_xor_b32_e32 v77, s8, v77
	v_lshl_or_b32 v76, v76, 5, v77
	v_lshl_add_u32 v60, v76, 2, s6
	s_and_saveexec_b64 s[4:5], vcc
	ds_add_rtn_u32 v44, v60, v79
	s_or_b64 exec, exec, s[4:5]
	s_waitcnt vmcnt(2)
	v_add_u32_e32 v76, 5120, v0
	v_lshl_add_u32 v76, v76, 1, 1
	v_cmp_gt_i32_e32 vcc, s33, v76
	v_lshrrev_b32_e32 v76, 25, v24
	v_bfe_u32 v77, v24, 13, 12
	v_min_u32_e32 v77, 31, v77
	v_xor_b32_e32 v77, s8, v77
	v_lshl_or_b32 v76, v76, 5, v77
	v_lshl_add_u32 v61, v76, 2, s6
	s_and_saveexec_b64 s[4:5], vcc
	ds_add_rtn_u32 v45, v61, v79
	s_or_b64 exec, exec, s[4:5]
	s_waitcnt vmcnt(1)
	v_add_u32_e32 v76, 6144, v0
	v_lshl_add_u32 v76, v76, 1, 0
	v_cmp_gt_i32_e32 vcc, s33, v76
	v_lshrrev_b32_e32 v76, 25, v26
	v_bfe_u32 v77, v26, 13, 12
	v_min_u32_e32 v77, 31, v77
	v_xor_b32_e32 v77, s8, v77
	v_lshl_or_b32 v76, v76, 5, v77
	v_lshl_add_u32 v62, v76, 2, s6
	s_and_saveexec_b64 s[4:5], vcc
	ds_add_rtn_u32 v46, v62, v79
	s_or_b64 exec, exec, s[4:5]
	s_waitcnt vmcnt(1)
	v_add_u32_e32 v76, 6144, v0
	v_lshl_add_u32 v76, v76, 1, 1
	v_cmp_gt_i32_e32 vcc, s33, v76
	v_lshrrev_b32_e32 v76, 25, v28
	v_bfe_u32 v77, v28, 13, 12
	v_min_u32_e32 v77, 31, v77
	v_xor_b32_e32 v77, s8, v77
	v_lshl_or_b32 v76, v76, 5, v77
	v_lshl_add_u32 v63, v76, 2, s6
	s_and_saveexec_b64 s[4:5], vcc
	ds_add_rtn_u32 v47, v63, v79
	s_or_b64 exec, exec, s[4:5]
	s_waitcnt vmcnt(0)
	v_add_u32_e32 v76, 7168, v0
	v_lshl_add_u32 v76, v76, 1, 0
	v_cmp_gt_i32_e32 vcc, s33, v76
	v_lshrrev_b32_e32 v76, 25, v30
	v_bfe_u32 v77, v30, 13, 12
	v_min_u32_e32 v77, 31, v77
	v_xor_b32_e32 v77, s8, v77
	v_lshl_or_b32 v76, v76, 5, v77
	v_lshl_add_u32 v64, v76, 2, s6
	s_and_saveexec_b64 s[4:5], vcc
	ds_add_rtn_u32 v48, v64, v79
	s_or_b64 exec, exec, s[4:5]
	s_waitcnt vmcnt(0)
	v_add_u32_e32 v76, 7168, v0
	v_lshl_add_u32 v76, v76, 1, 1
	v_cmp_gt_i32_e32 vcc, s33, v76
	v_lshrrev_b32_e32 v76, 25, v32
	v_bfe_u32 v77, v32, 13, 12
	v_min_u32_e32 v77, 31, v77
	v_xor_b32_e32 v77, s8, v77
	v_lshl_or_b32 v76, v76, 5, v77
	v_lshl_add_u32 v65, v76, 2, s6
	s_and_saveexec_b64 s[4:5], vcc
	ds_add_rtn_u32 v49, v65, v79
	s_or_b64 exec, exec, s[4:5]
	s_waitcnt lgkmcnt(0)
	s_barrier
	ds_read_b128 v[66:69], v1
	v_mbcnt_lo_u32_b32 v70, -1, 0
	v_mbcnt_hi_u32_b32 v70, -1, v70
	v_lshrrev_b32_e32 v71, 6, v0
	s_waitcnt lgkmcnt(0)
	v_add_u32_e32 v74, v66, v67
	v_add_u32_e32 v75, v74, v68
	v_add_u32_e32 v73, v75, v69
	v_mov_b32_e32 v72, v73
	v_subrev_u32_e32 v77, 1, v70
	v_lshlrev_b32_e32 v77, 2, v77
	ds_bpermute_b32 v76, v77, v72
	v_cmp_le_u32_e32 vcc, 1, v70
	s_waitcnt lgkmcnt(0)
	v_cndmask_b32_e32 v76, 0, v76, vcc
	v_add_u32_e32 v72, v72, v76
	v_subrev_u32_e32 v77, 2, v70
	v_lshlrev_b32_e32 v77, 2, v77
	ds_bpermute_b32 v76, v77, v72
	v_cmp_le_u32_e32 vcc, 2, v70
	s_waitcnt lgkmcnt(0)
	v_cndmask_b32_e32 v76, 0, v76, vcc
	v_add_u32_e32 v72, v72, v76
	v_subrev_u32_e32 v77, 4, v70
	v_lshlrev_b32_e32 v77, 2, v77
	ds_bpermute_b32 v76, v77, v72
	v_cmp_le_u32_e32 vcc, 4, v70
	s_waitcnt lgkmcnt(0)
	v_cndmask_b32_e32 v76, 0, v76, vcc
	v_add_u32_e32 v72, v72, v76
	v_subrev_u32_e32 v77, 8, v70
	v_lshlrev_b32_e32 v77, 2, v77
	ds_bpermute_b32 v76, v77, v72
	v_cmp_le_u32_e32 vcc, 8, v70
	s_waitcnt lgkmcnt(0)
	v_cndmask_b32_e32 v76, 0, v76, vcc
	v_add_u32_e32 v72, v72, v76
	v_subrev_u32_e32 v77, 16, v70
	v_lshlrev_b32_e32 v77, 2, v77
	ds_bpermute_b32 v76, v77, v72
	v_cmp_le_u32_e32 vcc, 16, v70
	s_waitcnt lgkmcnt(0)
	v_cndmask_b32_e32 v76, 0, v76, vcc
	v_add_u32_e32 v72, v72, v76
	v_subrev_u32_e32 v77, 32, v70
	v_lshlrev_b32_e32 v77, 2, v77
	ds_bpermute_b32 v76, v77, v72
	v_cmp_le_u32_e32 vcc, 32, v70
	s_waitcnt lgkmcnt(0)
	v_cndmask_b32_e32 v76, 0, v76, vcc
	v_add_u32_e32 v72, v72, v76
	s_mov_b32 s7, 0x24000
	v_lshl_add_u32 v77, v71, 2, s7
	v_cmp_eq_u32_e32 vcc, 63, v70
	s_and_saveexec_b64 s[4:5], vcc
	ds_write_b32 v77, v72
	s_or_b64 exec, exec, s[4:5]
	s_waitcnt lgkmcnt(0)
	s_barrier
	v_mov_b32_e32 v77, s7
	ds_read_b128 v[80:83], v77
	ds_read_b128 v[84:87], v77 offset:16
	ds_read_b128 v[88:91], v77 offset:32
	ds_read_b128 v[92:95], v77 offset:48
	v_mov_b32_e32 v78, 0
	s_waitcnt lgkmcnt(0)
	v_cmp_lt_u32_e32 vcc, 0, v71
	v_cndmask_b32_e32 v76, 0, v80, vcc
	v_add_u32_e32 v78, v78, v76
	v_cmp_lt_u32_e32 vcc, 1, v71
	v_cndmask_b32_e32 v76, 0, v81, vcc
	v_add_u32_e32 v78, v78, v76
	v_cmp_lt_u32_e32 vcc, 2, v71
	v_cndmask_b32_e32 v76, 0, v82, vcc
	v_add_u32_e32 v78, v78, v76
	v_cmp_lt_u32_e32 vcc, 3, v71
	v_cndmask_b32_e32 v76, 0, v83, vcc
	v_add_u32_e32 v78, v78, v76
	v_cmp_lt_u32_e32 vcc, 4, v71
	v_cndmask_b32_e32 v76, 0, v84, vcc
	v_add_u32_e32 v78, v78, v76
	v_cmp_lt_u32_e32 vcc, 5, v71
	v_cndmask_b32_e32 v76, 0, v85, vcc
	v_add_u32_e32 v78, v78, v76
	v_cmp_lt_u32_e32 vcc, 6, v71
	v_cndmask_b32_e32 v76, 0, v86, vcc
	v_add_u32_e32 v78, v78, v76
	v_cmp_lt_u32_e32 vcc, 7, v71
	v_cndmask_b32_e32 v76, 0, v87, vcc
	v_add_u32_e32 v78, v78, v76
	v_cmp_lt_u32_e32 vcc, 8, v71
	v_cndmask_b32_e32 v76, 0, v88, vcc
	v_add_u32_e32 v78, v78, v76
	v_cmp_lt_u32_e32 vcc, 9, v71
	v_cndmask_b32_e32 v76, 0, v89, vcc
	v_add_u32_e32 v78, v78, v76
	v_cmp_lt_u32_e32 vcc, 10, v71
	v_cndmask_b32_e32 v76, 0, v90, vcc
	v_add_u32_e32 v78, v78, v76
	v_cmp_lt_u32_e32 vcc, 11, v71
	v_cndmask_b32_e32 v76, 0, v91, vcc
	v_add_u32_e32 v78, v78, v76
	v_cmp_lt_u32_e32 vcc, 12, v71
	v_cndmask_b32_e32 v76, 0, v92, vcc
	v_add_u32_e32 v78, v78, v76
	v_cmp_lt_u32_e32 vcc, 13, v71
	v_cndmask_b32_e32 v76, 0, v93, vcc
	v_add_u32_e32 v78, v78, v76
	v_cmp_lt_u32_e32 vcc, 14, v71
	v_cndmask_b32_e32 v76, 0, v94, vcc
	v_add_u32_e32 v78, v78, v76
	v_sub_u32_e32 v72, v72, v73
	v_add_u32_e32 v72, v72, v78
	v_add_u32_e32 v76, v72, v66
	v_add_u32_e32 v77, v72, v74
	v_add_u32_e32 v78, v72, v75
	v_mov_b32_e32 v66, v72
	v_mov_b32_e32 v67, v76
	v_mov_b32_e32 v68, v77
	v_mov_b32_e32 v69, v78
	ds_write_b128 v1, v[66:69]
	v_and_b32_e32 v76, 7, v0
	v_lshrrev_b32_e32 v77, 3, v0
	v_lshl_add_u32 v77, s42, 7, v77
	v_cmp_eq_u32_e32 vcc, 0, v76
	v_cmp_gt_i32_e64 s[4:5], s44, v77
	s_and_b64 s[4:5], vcc, s[4:5]
	v_add_u32_e32 v78, s36, v72
	v_lshlrev_b32_e32 v76, 2, v77
	s_and_saveexec_b64 s[8:9], s[4:5]
	global_store_dword v76, v78, s[38:39]
	s_add_i32 s7, s44, -1
	v_cmp_eq_u32_e32 vcc, s7, v77
	s_and_b64 exec, exec, vcc
	v_mov_b32_e32 v78, s45
	global_store_dword v76, v78, s[38:39] offset:4
	s_mov_b64 exec, s[8:9]
	s_waitcnt lgkmcnt(0)
	s_barrier
	v_add_u32_e32 v76, 0, v0
	v_lshl_add_u32 v76, v76, 1, 0
	v_cmp_gt_i32_e32 vcc, s33, v76
	s_and_saveexec_b64 s[4:5], vcc
	ds_read_b32 v50, v50
	s_or_b64 exec, exec, s[4:5]
	v_add_u32_e32 v76, 0, v0
	v_lshl_add_u32 v76, v76, 1, 1
	v_cmp_gt_i32_e32 vcc, s33, v76
	s_and_saveexec_b64 s[4:5], vcc
	ds_read_b32 v51, v51
	s_or_b64 exec, exec, s[4:5]
	v_add_u32_e32 v76, 1024, v0
	v_lshl_add_u32 v76, v76, 1, 0
	v_cmp_gt_i32_e32 vcc, s33, v76
	s_and_saveexec_b64 s[4:5], vcc
	ds_read_b32 v52, v52
	s_or_b64 exec, exec, s[4:5]
	v_add_u32_e32 v76, 1024, v0
	v_lshl_add_u32 v76, v76, 1, 1
	v_cmp_gt_i32_e32 vcc, s33, v76
	s_and_saveexec_b64 s[4:5], vcc
	ds_read_b32 v53, v53
	s_or_b64 exec, exec, s[4:5]
	v_add_u32_e32 v76, 2048, v0
	v_lshl_add_u32 v76, v76, 1, 0
	v_cmp_gt_i32_e32 vcc, s33, v76
	s_and_saveexec_b64 s[4:5], vcc
	ds_read_b32 v54, v54
	s_or_b64 exec, exec, s[4:5]
	v_add_u32_e32 v76, 2048, v0
	v_lshl_add_u32 v76, v76, 1, 1
	v_cmp_gt_i32_e32 vcc, s33, v76
	s_and_saveexec_b64 s[4:5], vcc
	ds_read_b32 v55, v55
	s_or_b64 exec, exec, s[4:5]
	v_add_u32_e32 v76, 3072, v0
	v_lshl_add_u32 v76, v76, 1, 0
	v_cmp_gt_i32_e32 vcc, s33, v76
	s_and_saveexec_b64 s[4:5], vcc
	ds_read_b32 v56, v56
	s_or_b64 exec, exec, s[4:5]
	v_add_u32_e32 v76, 3072, v0
	v_lshl_add_u32 v76, v76, 1, 1
	v_cmp_gt_i32_e32 vcc, s33, v76
	s_and_saveexec_b64 s[4:5], vcc
	ds_read_b32 v57, v57
	s_or_b64 exec, exec, s[4:5]
	v_add_u32_e32 v76, 4096, v0
	v_lshl_add_u32 v76, v76, 1, 0
	v_cmp_gt_i32_e32 vcc, s33, v76
	s_and_saveexec_b64 s[4:5], vcc
	ds_read_b32 v58, v58
	s_or_b64 exec, exec, s[4:5]
	v_add_u32_e32 v76, 4096, v0
	v_lshl_add_u32 v76, v76, 1, 1
	v_cmp_gt_i32_e32 vcc, s33, v76
	s_and_saveexec_b64 s[4:5], vcc
	ds_read_b32 v59, v59
	s_or_b64 exec, exec, s[4:5]
	v_add_u32_e32 v76, 5120, v0
	v_lshl_add_u32 v76, v76, 1, 0
	v_cmp_gt_i32_e32 vcc, s33, v76
	s_and_saveexec_b64 s[4:5], vcc
	ds_read_b32 v60, v60
	s_or_b64 exec, exec, s[4:5]
	v_add_u32_e32 v76, 5120, v0
	v_lshl_add_u32 v76, v76, 1, 1
	v_cmp_gt_i32_e32 vcc, s33, v76
	s_and_saveexec_b64 s[4:5], vcc
	ds_read_b32 v61, v61
	s_or_b64 exec, exec, s[4:5]
	v_add_u32_e32 v76, 6144, v0
	v_lshl_add_u32 v76, v76, 1, 0
	v_cmp_gt_i32_e32 vcc, s33, v76
	s_and_saveexec_b64 s[4:5], vcc
	ds_read_b32 v62, v62
	s_or_b64 exec, exec, s[4:5]
	v_add_u32_e32 v76, 6144, v0
	v_lshl_add_u32 v76, v76, 1, 1
	v_cmp_gt_i32_e32 vcc, s33, v76
	s_and_saveexec_b64 s[4:5], vcc
	ds_read_b32 v63, v63
	s_or_b64 exec, exec, s[4:5]
	v_add_u32_e32 v76, 7168, v0
	v_lshl_add_u32 v76, v76, 1, 0
	v_cmp_gt_i32_e32 vcc, s33, v76
	s_and_saveexec_b64 s[4:5], vcc
	ds_read_b32 v64, v64
	s_or_b64 exec, exec, s[4:5]
	v_add_u32_e32 v76, 7168, v0
	v_lshl_add_u32 v76, v76, 1, 1
	v_cmp_gt_i32_e32 vcc, s33, v76
	s_and_saveexec_b64 s[4:5], vcc
	ds_read_b32 v65, v65
	s_or_b64 exec, exec, s[4:5]
	s_waitcnt lgkmcnt(0)
	s_barrier
	v_add_u32_e32 v76, 0, v0
	v_lshl_add_u32 v76, v76, 1, 0
	v_cmp_gt_i32_e32 vcc, s33, v76
	v_add_u32_e32 v77, v50, v34
	v_lshlrev_b32_e32 v77, 3, v77
	v_and_b32_e32 v2, 0x1ffffff, v2
	s_and_saveexec_b64 s[4:5], vcc
	ds_write_b64 v77, v[2:3]
	s_or_b64 exec, exec, s[4:5]
	v_add_u32_e32 v76, 0, v0
	v_lshl_add_u32 v76, v76, 1, 1
	v_cmp_gt_i32_e32 vcc, s33, v76
	v_add_u32_e32 v77, v51, v35
	v_lshlrev_b32_e32 v77, 3, v77
	v_and_b32_e32 v4, 0x1ffffff, v4
	s_and_saveexec_b64 s[4:5], vcc
	ds_write_b64 v77, v[4:5]
	s_or_b64 exec, exec, s[4:5]
	v_add_u32_e32 v76, 1024, v0
	v_lshl_add_u32 v76, v76, 1, 0
	v_cmp_gt_i32_e32 vcc, s33, v76
	v_add_u32_e32 v77, v52, v36
	v_lshlrev_b32_e32 v77, 3, v77
	v_and_b32_e32 v6, 0x1ffffff, v6
	s_and_saveexec_b64 s[4:5], vcc
	ds_write_b64 v77, v[6:7]
	s_or_b64 exec, exec, s[4:5]
	v_add_u32_e32 v76, 1024, v0
	v_lshl_add_u32 v76, v76, 1, 1
	v_cmp_gt_i32_e32 vcc, s33, v76
	v_add_u32_e32 v77, v53, v37
	v_lshlrev_b32_e32 v77, 3, v77
	v_and_b32_e32 v8, 0x1ffffff, v8
	s_and_saveexec_b64 s[4:5], vcc
	ds_write_b64 v77, v[8:9]
	s_or_b64 exec, exec, s[4:5]
	v_add_u32_e32 v76, 2048, v0
	v_lshl_add_u32 v76, v76, 1, 0
	v_cmp_gt_i32_e32 vcc, s33, v76
	v_add_u32_e32 v77, v54, v38
	v_lshlrev_b32_e32 v77, 3, v77
	v_and_b32_e32 v10, 0x1ffffff, v10
	s_and_saveexec_b64 s[4:5], vcc
	ds_write_b64 v77, v[10:11]
	s_or_b64 exec, exec, s[4:5]
	v_add_u32_e32 v76, 2048, v0
	v_lshl_add_u32 v76, v76, 1, 1
	v_cmp_gt_i32_e32 vcc, s33, v76
	v_add_u32_e32 v77, v55, v39
	v_lshlrev_b32_e32 v77, 3, v77
	v_and_b32_e32 v12, 0x1ffffff, v12
	s_and_saveexec_b64 s[4:5], vcc
	ds_write_b64 v77, v[12:13]
	s_or_b64 exec, exec, s[4:5]
	v_add_u32_e32 v76, 3072, v0
	v_lshl_add_u32 v76, v76, 1, 0
	v_cmp_gt_i32_e32 vcc, s33, v76
	v_add_u32_e32 v77, v56, v40
	v_lshlrev_b32_e32 v77, 3, v77
	v_and_b32_e32 v14, 0x1ffffff, v14
	s_and_saveexec_b64 s[4:5], vcc
	ds_write_b64 v77, v[14:15]
	s_or_b64 exec, exec, s[4:5]
	v_add_u32_e32 v76, 3072, v0
	v_lshl_add_u32 v76, v76, 1, 1
	v_cmp_gt_i32_e32 vcc, s33, v76
	v_add_u32_e32 v77, v57, v41
	v_lshlrev_b32_e32 v77, 3, v77
	v_and_b32_e32 v16, 0x1ffffff, v16
	s_and_saveexec_b64 s[4:5], vcc
	ds_write_b64 v77, v[16:17]
	s_or_b64 exec, exec, s[4:5]
	v_add_u32_e32 v76, 4096, v0
	v_lshl_add_u32 v76, v76, 1, 0
	v_cmp_gt_i32_e32 vcc, s33, v76
	v_add_u32_e32 v77, v58, v42
	v_lshlrev_b32_e32 v77, 3, v77
	v_and_b32_e32 v18, 0x1ffffff, v18
	s_and_saveexec_b64 s[4:5], vcc
	ds_write_b64 v77, v[18:19]
	s_or_b64 exec, exec, s[4:5]
	v_add_u32_e32 v76, 4096, v0
	v_lshl_add_u32 v76, v76, 1, 1
	v_cmp_gt_i32_e32 vcc, s33, v76
	v_add_u32_e32 v77, v59, v43
	v_lshlrev_b32_e32 v77, 3, v77
	v_and_b32_e32 v20, 0x1ffffff, v20
	s_and_saveexec_b64 s[4:5], vcc
	ds_write_b64 v77, v[20:21]
	s_or_b64 exec, exec, s[4:5]
	v_add_u32_e32 v76, 5120, v0
	v_lshl_add_u32 v76, v76, 1, 0
	v_cmp_gt_i32_e32 vcc, s33, v76
	v_add_u32_e32 v77, v60, v44
	v_lshlrev_b32_e32 v77, 3, v77
	v_and_b32_e32 v22, 0x1ffffff, v22
	s_and_saveexec_b64 s[4:5], vcc
	ds_write_b64 v77, v[22:23]
	s_or_b64 exec, exec, s[4:5]
	v_add_u32_e32 v76, 5120, v0
	v_lshl_add_u32 v76, v76, 1, 1
	v_cmp_gt_i32_e32 vcc, s33, v76
	v_add_u32_e32 v77, v61, v45
	v_lshlrev_b32_e32 v77, 3, v77
	v_and_b32_e32 v24, 0x1ffffff, v24
	s_and_saveexec_b64 s[4:5], vcc
	ds_write_b64 v77, v[24:25]
	s_or_b64 exec, exec, s[4:5]
	v_add_u32_e32 v76, 6144, v0
	v_lshl_add_u32 v76, v76, 1, 0
	v_cmp_gt_i32_e32 vcc, s33, v76
	v_add_u32_e32 v77, v62, v46
	v_lshlrev_b32_e32 v77, 3, v77
	v_and_b32_e32 v26, 0x1ffffff, v26
	s_and_saveexec_b64 s[4:5], vcc
	ds_write_b64 v77, v[26:27]
	s_or_b64 exec, exec, s[4:5]
	v_add_u32_e32 v76, 6144, v0
	v_lshl_add_u32 v76, v76, 1, 1
	v_cmp_gt_i32_e32 vcc, s33, v76
	v_add_u32_e32 v77, v63, v47
	v_lshlrev_b32_e32 v77, 3, v77
	v_and_b32_e32 v28, 0x1ffffff, v28
	s_and_saveexec_b64 s[4:5], vcc
	ds_write_b64 v77, v[28:29]
	s_or_b64 exec, exec, s[4:5]
	v_add_u32_e32 v76, 7168, v0
	v_lshl_add_u32 v76, v76, 1, 0
	v_cmp_gt_i32_e32 vcc, s33, v76
	v_add_u32_e32 v77, v64, v48
	v_lshlrev_b32_e32 v77, 3, v77
	v_and_b32_e32 v30, 0x1ffffff, v30
	s_and_saveexec_b64 s[4:5], vcc
	ds_write_b64 v77, v[30:31]
	s_or_b64 exec, exec, s[4:5]
	v_add_u32_e32 v76, 7168, v0
	v_lshl_add_u32 v76, v76, 1, 1
	v_cmp_gt_i32_e32 vcc, s33, v76
	v_add_u32_e32 v77, v65, v49
	v_lshlrev_b32_e32 v77, 3, v77
	v_and_b32_e32 v32, 0x1ffffff, v32
	s_and_saveexec_b64 s[4:5], vcc
	ds_write_b64 v77, v[32:33]
	s_or_b64 exec, exec, s[4:5]
	s_waitcnt lgkmcnt(0)
	s_barrier
	v_lshlrev_b32_e32 v8, 1, v0
	v_cmp_gt_i32_e32 vcc, s33, v8
	s_and_saveexec_b64 s[0:1], vcc
	s_cbranch_execz .LBB3_141
	v_add_u32_e32 v2, s36, v8
	v_ashrrev_i32_e32 v3, 31, v2
	v_lshl_add_u64 v[2:3], v[2:3], 3, s[40:41]
	v_lshlrev_b32_e32 v1, 4, v0
	s_mov_b64 s[0:1], 0
	s_mov_b64 s[2:3], 0x4000
.Ll2_copy:
	ds_read_b128 v[4:7], v1
	v_add_u32_e32 v9, 1, v8
	v_cmp_gt_i32_e32 vcc, s33, v9
	s_waitcnt lgkmcnt(0)
	s_mov_b64 s[4:5], exec
	s_and_b64 exec, s[4:5], vcc
	global_store_dwordx4 v[2:3], v[4:7], off
	s_andn2_b64 exec, s[4:5], vcc
	global_store_dwordx2 v[2:3], v[4:5], off
	s_mov_b64 exec, s[4:5]
	v_add_u32_e32 v8, 0x800, v8
	v_cmp_le_i32_e32 vcc, s33, v8
	v_add_u32_e32 v1, 0x4000, v1
	s_or_b64 s[0:1], vcc, s[0:1]
	v_lshl_add_u64 v[2:3], v[2:3], 0, s[2:3]
	s_andn2_b64 exec, exec, s[0:1]
	s_cbranch_execnz .Ll2_copy
